# MLA stream: waves 4-7 take the per-tile barrier at mid-tile (phase shift between SIMD partners), on the trimmed loops
# baseline (speedup 1.0000x reference)
.LBB0_695:
	v_add_f32_e32 v2, v208, v2
	v_add_f32_e32 v4, v209, v66
	v_add_f32_e32 v2, v4, v2
	v_add_f32_e32 v4, v84, v67
	v_add_f32_e32 v2, v4, v2
	v_add_f32_e32 v4, v85, v68
	v_add_f32_e32 v2, v4, v2
	v_add_f32_e32 v4, v86, v69
	v_add_f32_e32 v2, v4, v2
	v_add_f32_e32 v4, v87, v70
	v_add_f32_e32 v2, v4, v2
	v_add_f32_e32 v4, v88, v71
	v_add_f32_e32 v2, v4, v2
	v_add_f32_e32 v4, v89, v72
	v_add_f32_e32 v2, v4, v2
	v_add_f32_e32 v4, v90, v73
	v_add_f32_e32 v2, v4, v2
	v_add_f32_e32 v4, v91, v74
	v_add_f32_e32 v2, v4, v2
	v_add_f32_e32 v4, v95, v75
	v_add_f32_e32 v2, v4, v2
	v_add_f32_e32 v4, v77, v82
	v_add_f32_e32 v2, v4, v2
	v_add_f32_e32 v4, v76, v83
	v_add_f32_e32 v2, v4, v2
	v_add_f32_e32 v4, v96, v94
	v_add_f32_e32 v2, v4, v2
	v_add_f32_e32 v4, v79, v93
	s_add_i32 s10, s60, 1
	v_add_f32_e32 v2, v4, v2
	v_add_f32_e32 v4, v78, v92
	s_and_b32 s60, s10, 3
	s_waitcnt vmcnt(6) lgkmcnt(0)
	s_cmp_lt_u32 s61, 0x80
	s_cbranch_scc0 .Lmla_end_skip
	s_barrier
.Lmla_end_skip:
	s_add_i32 s10, s64, 1
	v_add_f32_e32 v2, v4, v2
	s_and_b32 s64, s10, 3
	s_add_i32 s73, s73, 1
	v_add_f32_e32 v191, v191, v2
	s_cmp_eq_u32 s71, s73
	s_cbranch_scc1 .LBB0_741

.LBB0_719:
	s_mul_i32 s26, s64, 0x5400
	v_add_u32_e32 v2, s26, v205
	s_waitcnt lgkmcnt(3)
	ds_read_b128 v[4:7], v2
	s_waitcnt lgkmcnt(1)
	ds_read_b128 v[8:11], v2 offset:32
	ds_read_b128 v[12:15], v2 offset:6656
	ds_read_b128 v[82:85], v2 offset:6688
	ds_read_b128 v[158:161], v2 offset:64
	ds_read_b128 v[162:165], v2 offset:96
	ds_read_b128 v[86:89], v2 offset:6720
	ds_read_b128 v[90:93], v2 offset:6752
	ds_read_b128 v[194:197], v2 offset:128
	ds_read_b128 v[208:211], v2 offset:160
	ds_read_b128 v[94:97], v2 offset:6784
	ds_read_b128 v[166:169], v2 offset:6816
	v_add_u32_e32 v2, s26, v206
	s_waitcnt lgkmcnt(9)
	v_mfma_f32_32x32x16_bf16 v[66:81], v[12:15], v[134:137], v[50:65]
	s_waitcnt lgkmcnt(8)
	v_mfma_f32_32x32x16_bf16 v[66:81], v[82:85], v[138:141], v[66:81]
	s_waitcnt lgkmcnt(5)
	v_mfma_f32_32x32x16_bf16 v[66:81], v[86:89], v[142:145], v[66:81]
	s_waitcnt lgkmcnt(4)
	v_mfma_f32_32x32x16_bf16 v[66:81], v[90:93], v[146:149], v[66:81]
	s_waitcnt lgkmcnt(1)
	v_mfma_f32_32x32x16_bf16 v[66:81], v[94:97], v[150:153], v[66:81]
	s_waitcnt lgkmcnt(0)
	v_mfma_f32_32x32x16_bf16 v[66:81], v[166:169], v[154:157], v[66:81]
	v_mfma_f32_32x32x16_bf16 v[82:97], v[4:7], v[134:137], v[50:65]
	v_mfma_f32_32x32x16_bf16 v[82:97], v[8:11], v[138:141], v[82:97]
	ds_read_b64_tr_b16 v[174:175], v2 offset:13312
	ds_read_b64_tr_b16 v[176:177], v2 offset:13824
	ds_read_b64_tr_b16 v[170:171], v2 offset:14336
	ds_read_b64_tr_b16 v[172:173], v2 offset:14848
	ds_read_b64_tr_b16 v[166:167], v2 offset:15360
	ds_read_b64_tr_b16 v[168:169], v2 offset:15872
	ds_read_b64_tr_b16 v[8:9], v2 offset:16384
	ds_read_b64_tr_b16 v[10:11], v2 offset:16896
	v_mfma_f32_32x32x16_bf16 v[82:97], v[158:161], v[142:145], v[82:97]
	v_mfma_f32_32x32x16_bf16 v[82:97], v[162:165], v[146:149], v[82:97]
	ds_read_b64_tr_b16 v[162:163], v2 offset:17408
	ds_read_b64_tr_b16 v[164:165], v2 offset:17920
	ds_read_b64_tr_b16 v[158:159], v2 offset:18432
	ds_read_b64_tr_b16 v[160:161], v2 offset:18944
	ds_read_b64_tr_b16 v[12:13], v2 offset:19456
	ds_read_b64_tr_b16 v[14:15], v2 offset:19968
	ds_read_b64_tr_b16 v[4:5], v2 offset:20480
	ds_read_b64_tr_b16 v[6:7], v2 offset:20992
	v_mfma_f32_32x32x16_bf16 v[82:97], v[194:197], v[150:153], v[82:97]
	v_mfma_f32_32x32x16_bf16 v[82:97], v[208:211], v[154:157], v[82:97]
	s_cmp_lt_u32 s61, 0x80
	s_cbranch_scc1 .Lmla_mid_skip
	s_and_b64 vcc, exec, s[10:11]
	s_cbranch_vccz .Lmla_mid_bg
	s_waitcnt vmcnt(6) lgkmcnt(0)
	s_branch .Lmla_mid_join
.Lmla_mid_bg:
	s_waitcnt vmcnt(14) lgkmcnt(0)

.Lmla_mid_skip:
	s_nop 4
	v_max3_f32 v194, v66, v67, v68
	v_max3_f32 v196, v69, v70, v71
	v_max3_f32 v194, v194, v72, v73
	v_max3_f32 v196, v196, v74, v75
	v_max3_f32 v194, v194, v76, v77
	v_max3_f32 v196, v196, v78, v79
	v_max3_f32 v194, v194, v196, v80
	v_max3_f32 v2, v82, v83, v84
	v_max3_f32 v195, v85, v86, v87
	v_max3_f32 v2, v2, v88, v89
	v_max3_f32 v195, v195, v90, v91
	v_max3_f32 v2, v2, v92, v93
	v_max3_f32 v195, v195, v94, v95
	v_max3_f32 v2, v2, v195, v96
	v_max_f32_e32 v195, v97, v81
	v_max3_f32 v2, v2, v194, v195
	ds_bpermute_b32 v194, v223, v2
	s_cmp_lg_u32 s73, 0
	s_waitcnt lgkmcnt(0)
	v_max_f32_e32 v208, v2, v194
	s_cbranch_scc0 .Lmla_f_first
	v_cmp_lt_f32_e32 vcc, s81, v208
	s_cbranch_vccz .LBB0_726
	v_max_f32_e32 v2, v208, v208
	v_max_f32_e32 v2, 0, v2
	s_branch .Lmla_f_resc

.LBB0_744:
	v_exp_f32_e32 v214, v16
	v_exp_f32_e32 v216, v17
	v_exp_f32_e32 v17, v84
	v_exp_f32_e32 v16, v85
	v_exp_f32_e32 v85, v86
	v_exp_f32_e32 v84, v87
	v_exp_f32_e32 v2, v82
	v_exp_f32_e32 v215, v83
	v_exp_f32_e32 v217, v66
	v_exp_f32_e32 v219, v67
	v_exp_f32_e32 v218, v68
	v_exp_f32_e32 v220, v69
	v_exp_f32_e32 v83, v70
	v_exp_f32_e32 v82, v71
	v_cvt_pk_bf16_f32 v66, v2, v215
	v_cvt_pk_bf16_f32 v67, v217, v219
	v_cvt_pk_bf16_f32 v68, v17, v16
	v_cvt_pk_bf16_f32 v69, v85, v84
	v_exp_f32_e32 v87, v88
	v_exp_f32_e32 v86, v89
	v_mfma_f32_32x32x16_bf16 v[34:49], v[174:177], v[66:69], v[34:49]
	v_exp_f32_e32 v89, v90
	v_exp_f32_e32 v88, v91
	v_exp_f32_e32 v91, v92
	v_exp_f32_e32 v90, v93
	v_exp_f32_e32 v93, v94
	v_exp_f32_e32 v92, v95
	v_exp_f32_e32 v97, v72
	v_exp_f32_e32 v96, v73
	v_exp_f32_e32 v195, v74
	v_exp_f32_e32 v194, v75
	v_cvt_pk_bf16_f32 v70, v87, v86
	v_cvt_pk_bf16_f32 v71, v89, v88
	v_cvt_pk_bf16_f32 v72, v91, v90
	v_cvt_pk_bf16_f32 v73, v93, v92
	v_mfma_f32_32x32x16_bf16 v[18:33], v[158:161], v[66:69], v[18:33]
	v_exp_f32_e32 v197, v76
	v_exp_f32_e32 v196, v77
	v_exp_f32_e32 v211, v78
	v_exp_f32_e32 v210, v79
	v_cvt_pk_bf16_f32 v74, v214, v216
	v_mfma_f32_32x32x16_bf16 v[34:49], v[170:173], v[70:73], v[34:49]
	v_cvt_pk_bf16_f32 v75, v218, v220
	v_cvt_pk_bf16_f32 v76, v83, v82
	v_cvt_pk_bf16_f32 v77, v97, v96
	v_exp_f32_e32 v213, v80
	v_exp_f32_e32 v212, v81
	v_mfma_f32_32x32x16_bf16 v[18:33], v[12:15], v[70:73], v[18:33]
	v_cvt_pk_bf16_f32 v78, v195, v194
	v_cvt_pk_bf16_f32 v79, v197, v196
	v_add_f32_e32 v2, v214, v2
	v_cvt_pk_bf16_f32 v80, v211, v210
	v_cvt_pk_bf16_f32 v81, v213, v212
	v_mfma_f32_32x32x16_bf16 v[34:49], v[166:169], v[74:77], v[34:49]
	v_add_f32_e32 v94, v216, v215
	v_add_f32_e32 v95, v218, v217
	v_add_f32_e32 v2, v94, v2
	v_add_f32_e32 v2, v95, v2
	v_pk_add_f32 v[16:17], v[82:83], v[16:17]
	v_pk_add_f32 v[66:67], v[96:97], v[84:85]
	v_mfma_f32_32x32x16_bf16 v[18:33], v[8:11], v[74:77], v[18:33]
	v_add_f32_e64 v68, v194, v86
	v_add_f32_e64 v69, v195, v87
	v_add_f32_e64 v82, v196, v88
	v_add_f32_e64 v83, v197, v89
	v_add_f32_e64 v84, v210, v90
	v_add_f32_e64 v85, v211, v91
	s_add_i32 s10, s60, 1
	v_pk_add_f32 v[86:87], v[212:213], v[92:93]
	s_and_b32 s60, s10, 3
	s_waitcnt vmcnt(6) lgkmcnt(0)
	v_mfma_f32_32x32x16_bf16 v[34:49], v[162:165], v[78:81], v[34:49]
	v_add_f32_e32 v162, v220, v219
	v_add_f32_e32 v2, v162, v2
	v_add_f32_e32 v2, v17, v2
	v_add_f32_e32 v2, v16, v2
	v_add_f32_e32 v2, v67, v2
	v_add_f32_e32 v2, v66, v2
	v_add_f32_e32 v2, v69, v2
	v_add_f32_e32 v2, v68, v2
	v_mfma_f32_32x32x16_bf16 v[18:33], v[4:7], v[78:81], v[18:33]
	v_add_f32_e32 v2, v83, v2
	v_add_f32_e32 v2, v82, v2
	v_add_f32_e32 v2, v85, v2
	v_add_f32_e32 v2, v84, v2
	v_add_f32_e32 v2, v87, v2
	s_cmp_lt_u32 s61, 0x80
	s_cbranch_scc0 .Lmla_mend_skip
	s_barrier
.Lmla_mend_skip:
	s_add_i32 s10, s64, 1
	v_add_f32_e32 v2, v86, v2
	s_and_b32 s64, s10, 3
	s_add_i32 s35, s35, 1
	v_add_f32_e32 v191, v191, v2
	s_cmp_ge_i32 s35, s34
	v_add_u32_e32 v209, 64, v209
	s_cbranch_scc1 .LBB0_765

.LBB0_756:
	s_mul_i32 s26, s64, 0x5400
	v_add_u32_e32 v2, s26, v205
	s_waitcnt lgkmcnt(3)
	ds_read_b128 v[4:7], v2 offset:6656
	s_waitcnt lgkmcnt(1)
	ds_read_b128 v[8:11], v2
	ds_read_b128 v[12:15], v2 offset:32
	ds_read_b128 v[158:161], v2 offset:6688
	ds_read_b128 v[162:165], v2 offset:64
	ds_read_b128 v[166:169], v2 offset:6720
	ds_read_b128 v[170:173], v2 offset:96
	ds_read_b128 v[174:177], v2 offset:6752
	ds_read_b128 v[194:197], v2 offset:128
	ds_read_b128 v[210:213], v2 offset:6784
	ds_read_b128 v[214:217], v2 offset:160
	ds_read_b128 v[218:221], v2 offset:6816
	s_waitcnt lgkmcnt(10)
	v_mfma_f32_32x32x16_bf16 v[82:97], v[8:11], v[134:137], v[50:65]
	v_mfma_f32_32x32x16_bf16 v[66:81], v[4:7], v[134:137], v[50:65]
	v_add_u32_e32 v6, s26, v206
	s_waitcnt lgkmcnt(9)
	v_mfma_f32_32x32x16_bf16 v[82:97], v[12:15], v[138:141], v[82:97]
	s_waitcnt lgkmcnt(8)
	v_mfma_f32_32x32x16_bf16 v[66:81], v[158:161], v[138:141], v[66:81]
	s_waitcnt lgkmcnt(7)
	v_mfma_f32_32x32x16_bf16 v[82:97], v[162:165], v[142:145], v[82:97]
	s_waitcnt lgkmcnt(6)
	v_mfma_f32_32x32x16_bf16 v[66:81], v[166:169], v[142:145], v[66:81]
	s_waitcnt lgkmcnt(5)
	v_mfma_f32_32x32x16_bf16 v[82:97], v[170:173], v[146:149], v[82:97]
	s_waitcnt lgkmcnt(4)
	v_mfma_f32_32x32x16_bf16 v[66:81], v[174:177], v[146:149], v[66:81]
	ds_read_b64_tr_b16 v[174:175], v6 offset:13312
	ds_read_b64_tr_b16 v[176:177], v6 offset:13824
	ds_read_b64_tr_b16 v[170:171], v6 offset:14336
	ds_read_b64_tr_b16 v[172:173], v6 offset:14848
	ds_read_b64_tr_b16 v[166:167], v6 offset:15360
	ds_read_b64_tr_b16 v[168:169], v6 offset:15872
	ds_read_b64_tr_b16 v[162:163], v6 offset:16384
	ds_read_b64_tr_b16 v[164:165], v6 offset:16896
	ds_read_b64_tr_b16 v[158:159], v6 offset:17408
	ds_read_b64_tr_b16 v[160:161], v6 offset:17920
	ds_read_b64_tr_b16 v[12:13], v6 offset:18432
	ds_read_b64_tr_b16 v[14:15], v6 offset:18944
	ds_read_b64_tr_b16 v[8:9], v6 offset:19456
	ds_read_b64_tr_b16 v[10:11], v6 offset:19968
	ds_read_b64_tr_b16 v[4:5], v6 offset:20480
	ds_read_b64_tr_b16 v[6:7], v6 offset:20992
	s_waitcnt lgkmcnt(14)
	v_mfma_f32_32x32x16_bf16 v[82:97], v[194:197], v[150:153], v[82:97]
	v_mfma_f32_32x32x16_bf16 v[66:81], v[210:213], v[150:153], v[66:81]
	v_mfma_f32_32x32x16_bf16 v[82:97], v[214:217], v[154:157], v[82:97]
	v_mfma_f32_32x32x16_bf16 v[66:81], v[218:221], v[154:157], v[66:81]
	s_cmp_lt_u32 s61, 0x80
	s_cbranch_scc1 .Lmla_mmid_skip
	s_waitcnt vmcnt(6) lgkmcnt(0)
	s_barrier
.Lmla_mmid_skip:
	v_sub_u32_e32 v222, v208, v209
	v_add_u32_e32 v222, 59, v222
	s_cmp_lg_u32 s35, -1
	v_cmp_ge_i32_e64 vcc, v222, 32
	v_cmp_ge_i32_e64 s[28:29], v222, 1
	v_cmp_ge_i32_e64 s[30:31], v222, 0
	s_nop 5
	v_cndmask_b32_e64 v16, v243, v66, vcc
	v_cmp_ge_i32_e64 vcc, v222, 33
	v_cndmask_b32_e64 v83, v243, v83, s[28:29]
	v_cmp_ge_i32_e64 s[28:29], v222, 2
	v_cndmask_b32_e64 v82, v243, v82, s[30:31]
	v_cmp_ge_i32_e64 s[30:31], v222, 34
	v_cndmask_b32_e64 v17, v243, v67, vcc
	v_cmp_ge_i32_e64 vcc, v222, 3
	v_cndmask_b32_e64 v66, v243, v84, s[28:29]
	v_cmp_ge_i32_e64 s[28:29], v222, 35
	v_cndmask_b32_e64 v68, v243, v68, s[30:31]
	v_cmp_ge_i32_e64 s[30:31], v222, 8
	v_cndmask_b32_e64 v67, v243, v85, vcc
	v_cmp_ge_i32_e64 vcc, v222, 40
	v_cndmask_b32_e64 v69, v243, v69, s[28:29]
	v_cmp_ge_i32_e64 s[28:29], v222, 9
	v_cndmask_b32_e64 v84, v243, v86, s[30:31]
	v_cmp_ge_i32_e64 s[30:31], v222, 41
	v_cndmask_b32_e64 v70, v243, v70, vcc
	v_cmp_ge_i32_e64 vcc, v222, 10
	v_cndmask_b32_e64 v85, v243, v87, s[28:29]
	v_cmp_ge_i32_e64 s[28:29], v222, 42
	v_cndmask_b32_e64 v71, v243, v71, s[30:31]
	v_cmp_ge_i32_e64 s[30:31], v222, 11
	v_cndmask_b32_e64 v86, v243, v88, vcc
	v_cmp_ge_i32_e64 vcc, v222, 43
	v_cndmask_b32_e64 v72, v243, v72, s[28:29]
	v_cmp_ge_i32_e64 s[28:29], v222, 16
	v_cndmask_b32_e64 v87, v243, v89, s[30:31]
	v_cmp_ge_i32_e64 s[30:31], v222, 48
	v_cndmask_b32_e64 v73, v243, v73, vcc
	v_cmp_ge_i32_e64 vcc, v222, 17
	v_cndmask_b32_e64 v88, v243, v90, s[28:29]
	v_cmp_ge_i32_e64 s[28:29], v222, 49
	v_cndmask_b32_e64 v74, v243, v74, s[30:31]
	v_cmp_ge_i32_e64 s[30:31], v222, 18
	v_cndmask_b32_e64 v89, v243, v91, vcc
	v_cmp_ge_i32_e64 vcc, v222, 50
	v_cndmask_b32_e64 v75, v243, v75, s[28:29]
	v_cmp_ge_i32_e64 s[28:29], v222, 19
	v_cndmask_b32_e64 v90, v243, v92, s[30:31]
	v_cmp_ge_i32_e64 s[30:31], v222, 51
	v_cndmask_b32_e64 v76, v243, v76, vcc
	v_cmp_ge_i32_e64 vcc, v222, 24
	v_cndmask_b32_e64 v91, v243, v93, s[28:29]
	v_cmp_ge_i32_e64 s[28:29], v222, 56
	v_cndmask_b32_e64 v77, v243, v77, s[30:31]
	v_cmp_ge_i32_e64 s[30:31], v222, 25
	v_cndmask_b32_e64 v92, v243, v94, vcc
	v_cmp_ge_i32_e64 vcc, v222, 57
	v_cndmask_b32_e64 v78, v243, v78, s[28:29]
	v_cmp_ge_i32_e64 s[28:29], v222, 26
	v_cndmask_b32_e64 v93, v243, v95, s[30:31]
	v_cmp_ge_i32_e64 s[30:31], v222, 58
	v_cndmask_b32_e64 v79, v243, v79, vcc
	v_cmp_ge_i32_e64 vcc, v222, 27
	v_cndmask_b32_e64 v94, v243, v96, s[28:29]
	v_cmp_ge_i32_e64 s[28:29], v222, 59
	v_cndmask_b32_e64 v80, v243, v80, s[30:31]
	v_cndmask_b32_e64 v95, v243, v97, vcc
	v_cndmask_b32_e64 v81, v243, v81, s[28:29]
	v_max3_f32 v96, v16, v17, v68
	v_max3_f32 v2, v82, v83, v66
	v_max3_f32 v2, v2, v67, v84
	v_max3_f32 v96, v96, v69, v70
	v_max3_f32 v2, v2, v85, v86
	v_max3_f32 v96, v96, v71, v72
	v_max3_f32 v2, v2, v87, v88
	v_max3_f32 v96, v96, v73, v74
	v_max3_f32 v2, v2, v89, v90
	v_max3_f32 v96, v96, v75, v76
	v_max3_f32 v2, v2, v91, v92
	v_max3_f32 v96, v96, v77, v78
	v_max3_f32 v2, v2, v93, v94
	v_max3_f32 v96, v96, v79, v80
	v_max_f32_e32 v97, v95, v81
	v_max3_f32 v2, v2, v96, v97
	ds_bpermute_b32 v96, v223, v2
	s_waitcnt lgkmcnt(0)
	v_max_f32_e32 v96, v2, v96
	s_cbranch_scc0 .Lmla_m_first
	v_cmp_lt_f32_e32 vcc, s81, v96
	s_cbranch_vccz .LBB0_744
	v_max_f32_e32 v2, v96, v96
	v_max_f32_e32 v2, 0, v2
	s_branch .Lmla_m_resc
